# stack + incremental (cached) weight-conversion addresses in the scan loop for both items, plus dead SGPR-reload removal in the loop
# speedup vs baseline: 1.0127x; 1.0008x over previous
.LBB0_422:
	s_and_b32 s98, s7, 31
	s_cmp_eq_u32 s98, 0
	s_cbranch_scc1 .Lcv1_slow
	v_readlane_b32 s100, v255, 44
	v_readlane_b32 s101, v255, 45
	s_add_u32 s100, s100, 0x1000000
	s_addc_u32 s101, s101, 0
	s_branch .Lcv1_go

.Lcv1_go:
	v_writelane_b32 v255, s100, 44
	v_writelane_b32 v255, s101, 45
	global_load_dwordx4 v[152:155], v250, s[100:101]
	v_add_u32_e32 v253, 0x2000, v250
	global_load_dwordx4 v[156:159], v253, s[100:101]
	v_add_u32_e32 v252, 0x4000, v250
	global_load_dwordx4 v[160:163], v252, s[100:101]
	v_add_u32_e32 v253, 0x6000, v250
	global_load_dwordx4 v[164:167], v253, s[100:101]
	v_add_u32_e32 v252, 0x8000, v250
	global_load_dwordx4 v[168:171], v252, s[100:101]
	v_add_u32_e32 v253, 0xa000, v250
	global_load_dwordx4 v[172:175], v253, s[100:101]
	v_add_u32_e32 v252, 0xc000, v250
	global_load_dwordx4 v[176:179], v252, s[100:101]
	v_add_u32_e32 v253, 0xe000, v250
	global_load_dwordx4 v[246:249], v253, s[100:101]
	s_cmp_lt_u32 s7, 30
	s_cselect_b64 s[94:95], -1, 0
	s_and_b64 s[0:1], s[94:95], exec
	s_cselect_b32 s0, s49, 0
	s_add_i32 s0, s0, s44
	s_lshl_b32 s0, s0, 3
	v_readlane_b32 s1, v255, 15
	s_add_i32 s28, s1, s0
	s_bfe_u32 s93, s28, 0x5000b
	s_ashr_i32 s57, s28, 16
	s_lshl_b32 s13, s93, 22
	s_cmp_eq_u32 s57, 3
	s_cselect_b64 s[96:97], -1, 0
	s_cmp_eq_u32 s93, 0
	s_cselect_b64 s[0:1], -1, 0
	s_lshl_b32 s34, s28, 5
	s_and_b32 s37, s34, 0x7e0
	s_and_b32 s36, s28, 0x7c0
	s_mov_b32 s38, s86
	s_cmp_gt_u32 s7, 29
	s_nop 4
	v_readlane_b32 s62, v254, 22
	s_nop 7
	s_cbranch_scc1 .LBB0_424
	s_sub_u32 s98, s7, 1
	s_cmp_lt_u32 s98, 27
	s_cbranch_scc0 .Lcv2_slow
	v_readlane_b32 s100, v255, 48
	v_readlane_b32 s101, v255, 49
	s_add_u32 s100, s100, 0x1000000
	s_addc_u32 s101, s101, 0
	s_branch .Lcv2_go
.Lcv2_slow:
	v_readlane_b32 s80, v254, 36
	s_cmp_eq_u32 s57, 1
	v_readlane_b32 s81, v254, 37
	v_readlane_b32 s82, v254, 38
	v_readlane_b32 s83, v254, 39
	s_cselect_b32 s29, s80, s82
	s_cselect_b32 s30, s81, s83
	s_nop 0
	s_cmp_lt_u32 s28, 0x10000
	v_readlane_b32 s82, v254, 58
	v_readlane_b32 s83, v254, 59
	s_cselect_b32 s28, s83, s30
	s_cselect_b32 s29, s82, s29
	s_lshl_b32 s30, s13, 2
	s_nop 6
	s_add_u32 s30, s29, s30
	s_addc_u32 s31, s28, 0
	s_nop 0
	v_readlane_b32 s78, v254, 54
	v_readlane_b32 s79, v254, 55
	s_and_b64 s[28:29], s[0:1], exec
	v_readlane_b32 s74, v254, 34
	v_readlane_b32 s75, v254, 35
	s_cselect_b32 s60, s74, s78
	s_cselect_b32 vcc_lo, s75, s79
	s_and_b64 s[28:29], s[96:97], exec
	s_cselect_b32 s29, vcc_lo, s31
	s_cselect_b32 s28, s60, s30
	s_lshl_b32 s98, s36, 13
	s_lshl_b32 s40, s37, 2
	s_add_u32 s98, s98, s40
	s_add_u32 s100, s28, s98
	s_addc_u32 s101, s29, 0
.Lcv2_go:
	v_writelane_b32 v255, s100, 48
	v_writelane_b32 v255, s101, 49
	global_load_dwordx4 v[2:5], v250, s[100:101]
	v_add_u32_e32 v253, 0x2000, v250
	global_load_dwordx4 v[6:9], v253, s[100:101]
	v_add_u32_e32 v252, 0x4000, v250
	global_load_dwordx4 v[10:13], v252, s[100:101]
	v_add_u32_e32 v253, 0x6000, v250
	global_load_dwordx4 v[14:17], v253, s[100:101]
	v_add_u32_e32 v252, 0x8000, v250
	global_load_dwordx4 v[18:21], v252, s[100:101]
	v_add_u32_e32 v253, 0xa000, v250
	global_load_dwordx4 v[22:25], v253, s[100:101]
	v_add_u32_e32 v252, 0xc000, v250
	global_load_dwordx4 v[26:29], v252, s[100:101]
	v_add_u32_e32 v253, 0xe000, v250
	global_load_dwordx4 v[116:119], v253, s[100:101]
	s_nop 7
	v_readlane_b32 s62, v254, 22
	s_nop 7

.LBB0_455:
	s_and_b32 s98, s47, 0x7c0
	s_cmp_eq_u32 s98, 0
	s_cbranch_scc1 .Lcv1f_slow
	v_readlane_b32 s100, v255, 46
	v_readlane_b32 s101, v255, 47
	v_readlane_b32 s98, v255, 52
	s_add_u32 s100, s100, s98
	s_addc_u32 s101, s101, 0
	s_branch .Lcv1f_go
.Lcv1f_slow:
	s_lshl_b32 s7, s92, 22
	s_lshl_b32 s7, s7, 1
	s_add_u32 s7, s35, s7
	s_addc_u32 s28, s33, 0
	s_add_u32 s29, s56, s12
	s_addc_u32 s30, s39, 0
	s_cmp_eq_u32 s11, 2
	s_cselect_b32 s7, s7, s29
	s_cselect_b32 s30, s28, s30
	s_and_b64 s[28:29], s[90:91], exec
	s_mov_b32 s12, 0x2400000
	s_nop 0
	s_cselect_b32 s28, s12, 0x4300000
	v_readlane_b32 s86, v254, 42
	v_readlane_b32 s87, v254, 43
	s_add_u32 s31, s86, s28
	s_addc_u32 s60, s87, 0
	s_and_b64 s[28:29], s[52:53], exec
	s_cselect_b32 s29, s60, s30
	s_cselect_b32 s28, s31, s7
	s_lshl_b32 s7, s43, 1
	s_and_b32 s30, s46, 0x60
	s_lshl_b32 s31, s11, 7
	s_and_b32 s7, s7, 0xf00
	s_or_b32 s30, s31, s30
	s_add_i32 s30, s30, s7
	s_cmp_gt_i32 s11, 1
	s_cselect_b32 s7, s43, s30
	s_ashr_i32 s11, s7, 3
	s_andn2_b32 s11, s11, 31
	s_or_b32 s30, s11, s50
	s_ashr_i32 s31, s30, 31
	s_lshl_b64 s[30:31], s[30:31], 8
	s_and_b32 s7, s7, 0xe0
	s_or_b32 s7, s30, s7
	s_mov_b32 s100, s7
	s_mov_b32 s101, s31
	s_lshl_b64 s[100:101], s[100:101], 7
	s_add_u32 s100, s100, s28
	s_addc_u32 s101, s101, s29
	s_ashr_i32 s98, s51, 16
	s_cmp_eq_u32 s98, 2
	s_mov_b32 s98, 0x1000000
	s_cselect_b32 s98, 0x800000, s98
	v_writelane_b32 v255, s98, 52
.Lcv1f_go:
	v_writelane_b32 v255, s100, 46
	v_writelane_b32 v255, s101, 47
	s_waitcnt vmcnt(1)
	v_cvt_pk_bf16_f32 v152, v152, v156
	v_cvt_pk_bf16_f32 v156, v153, v157
	v_cvt_pk_bf16_f32 v238, v154, v158
	v_cvt_pk_bf16_f32 v242, v155, v159
	v_cvt_pk_bf16_f32 v153, v160, v164
	v_cvt_pk_bf16_f32 v157, v161, v165
	v_cvt_pk_bf16_f32 v239, v162, v166
	v_cvt_pk_bf16_f32 v243, v163, v167
	v_cvt_pk_bf16_f32 v154, v168, v172
	v_cvt_pk_bf16_f32 v158, v169, v173
	v_cvt_pk_bf16_f32 v240, v170, v174
	v_cvt_pk_bf16_f32 v244, v171, v175
	v_cvt_pk_bf16_f32 v155, v176, v246
	v_cvt_pk_bf16_f32 v159, v177, v247
	v_cvt_pk_bf16_f32 v241, v178, v248
	v_cvt_pk_bf16_f32 v245, v179, v249
	global_store_dwordx4 v251, v[152:155], s[100:101]
	global_store_dwordx4 v251, v[156:159], s[100:101] offset:128
	global_store_dwordx4 v251, v[238:241], s[100:101] offset:256
	global_store_dwordx4 v251, v[242:245], s[100:101] offset:384
	s_andn2_b64 vcc, exec, s[94:95]
	s_mov_b32 s86, s38
	s_nop 4
	s_cbranch_vccnz .LBB0_410
	s_sub_u32 s98, s47, 64
	s_cmp_lt_u32 s98, 0x6c0
	s_cbranch_scc0 .Lcv2f_slow
	v_readlane_b32 s100, v255, 50
	v_readlane_b32 s101, v255, 51
	s_add_u32 s100, s100, 0x800000
	s_addc_u32 s101, s101, 0
	s_branch .Lcv2f_go
.Lcv2f_slow:
	s_lshl_b32 s7, s13, 1
	s_add_u32 s7, s35, s7
	s_addc_u32 s11, s33, 0
	s_lshl_b32 s28, s93, 24
	s_add_u32 s28, s56, s28
	s_addc_u32 s29, s39, 0
	s_cmp_eq_u32 s57, 2
	s_cselect_b32 s7, s7, s28
	s_cselect_b32 s11, s11, s29
	s_and_b64 s[0:1], s[0:1], exec
	s_mov_b32 s0, 0x2400000
	s_nop 0
	s_cselect_b32 s0, s0, 0x4300000
	v_readlane_b32 s78, v254, 42
	v_readlane_b32 s79, v254, 43
	s_add_u32 s28, s78, s0
	s_addc_u32 s29, s79, 0
	s_and_b64 s[0:1], s[96:97], exec
	s_cselect_b32 s1, s29, s11
	s_cselect_b32 s0, s28, s7
	s_lshl_b32 s7, s37, 1
	s_and_b32 s11, s34, 0x60
	s_lshl_b32 s28, s57, 7
	s_and_b32 s7, s7, 0xf00
	s_or_b32 s11, s28, s11
	s_add_i32 s11, s11, s7
	s_cmp_gt_i32 s57, 1
	s_cselect_b32 s7, s37, s11
	s_ashr_i32 s11, s7, 3
	s_andn2_b32 s11, s11, 31
	s_lshr_b32 s28, s36, 6
	s_or_b32 s28, s11, s28
	s_ashr_i32 s29, s28, 31
	s_lshl_b64 s[28:29], s[28:29], 8
	s_and_b32 s7, s7, 0xe0
	s_or_b32 s7, s28, s7
	s_nop 4
	s_mov_b32 s100, s7
	s_mov_b32 s101, s29
	s_lshl_b64 s[100:101], s[100:101], 7
	s_add_u32 s100, s100, s0
	s_addc_u32 s101, s101, s1
.Lcv2f_go:
	v_writelane_b32 v255, s100, 50
	v_writelane_b32 v255, s101, 51
	v_cvt_pk_bf16_f32 v2, v2, v6
	v_cvt_pk_bf16_f32 v6, v3, v7
	v_cvt_pk_bf16_f32 v238, v4, v8
	v_cvt_pk_bf16_f32 v242, v5, v9
	v_cvt_pk_bf16_f32 v3, v10, v14
	v_cvt_pk_bf16_f32 v7, v11, v15
	v_cvt_pk_bf16_f32 v239, v12, v16
	v_cvt_pk_bf16_f32 v243, v13, v17
	v_cvt_pk_bf16_f32 v4, v18, v22
	v_cvt_pk_bf16_f32 v8, v19, v23
	v_cvt_pk_bf16_f32 v240, v20, v24
	v_cvt_pk_bf16_f32 v244, v21, v25
	v_cvt_pk_bf16_f32 v5, v26, v116
	v_cvt_pk_bf16_f32 v9, v27, v117
	v_cvt_pk_bf16_f32 v241, v28, v118
	v_cvt_pk_bf16_f32 v245, v29, v119
	global_store_dwordx4 v251, v[2:5], s[100:101]
	global_store_dwordx4 v251, v[6:9], s[100:101] offset:128
	global_store_dwordx4 v251, v[238:241], s[100:101] offset:256
	global_store_dwordx4 v251, v[242:245], s[100:101] offset:384
	s_branch .LBB0_410
